# baseline (speedup 1.0000x reference)
.LBB1_4:
	v_add_u32_e32 v182, s19, v191
	v_add_u32_e32 v238, s19, v192
	ds_read_b128 v[178:181], v182 offset:32768
	ds_read_b128 v[194:197], v182 offset:34816
	ds_read_b128 v[198:201], v182 offset:36864
	ds_read_b128 v[202:205], v182 offset:38912
	ds_read_b128 v[206:209], v238
	ds_read_b128 v[210:213], v238 offset:2048
	ds_read_b128 v[214:217], v238 offset:4096
	ds_read_b128 v[218:221], v238 offset:6144
	ds_read_b128 v[222:225], v238 offset:8192
	ds_read_b128 v[226:229], v238 offset:10240
	ds_read_b128 v[230:233], v238 offset:12288
	ds_read_b128 v[234:237], v238 offset:14336
	s_min_u32 s21, s20, 29
	s_xor_b32 s19, s19, 0x10000
	v_add_u32_e32 v239, s19, v189
	s_waitcnt vmcnt(11)
	v_cvt_pk_bf16_f32 v13, v12, v13
	v_cvt_pk_bf16_f32 v12, v10, v11
	s_waitcnt vmcnt(10)
	v_cvt_pk_bf16_f32 v11, v20, v21
	v_cvt_pk_bf16_f32 v10, v18, v19
	ds_write2st64_b64 v239, v[12:13], v[10:11] offset1:8
	s_waitcnt vmcnt(9)
	v_cvt_pk_bf16_f32 v11, v24, v25
	v_cvt_pk_bf16_f32 v10, v22, v23
	s_waitcnt vmcnt(8)
	v_cvt_pk_bf16_f32 v13, v32, v33
	v_cvt_pk_bf16_f32 v12, v30, v31
	ds_write2st64_b64 v239, v[10:11], v[12:13] offset0:16 offset1:24
	s_waitcnt vmcnt(7)
	v_cvt_pk_bf16_f32 v11, v36, v37
	v_cvt_pk_bf16_f32 v10, v34, v35
	s_waitcnt vmcnt(6)
	v_cvt_pk_bf16_f32 v13, v40, v41
	v_cvt_pk_bf16_f32 v12, v38, v39
	ds_write2st64_b64 v239, v[10:11], v[12:13] offset0:32 offset1:40
	s_waitcnt vmcnt(5)
	v_cvt_pk_bf16_f32 v11, v44, v45
	v_cvt_pk_bf16_f32 v10, v42, v43
	s_waitcnt vmcnt(4)
	v_cvt_pk_bf16_f32 v13, v48, v49
	v_cvt_pk_bf16_f32 v12, v46, v47
	ds_write2st64_b64 v239, v[10:11], v[12:13] offset0:48 offset1:56
	s_waitcnt lgkmcnt(0)
	s_add_i32 s21, s21, 2
	s_barrier
	s_waitcnt lgkmcnt(11)
	v_mfma_f32_16x16x32_bf16 v[174:177], v[178:181], v[206:209], v[174:177]
	s_lshl_b32 s22, s21, 1
	s_and_b32 s22, s22, 0x60
	s_add_i32 s22, s22, s12
	s_lshl_b32 s22, s22, 6
	v_mfma_f32_16x16x32_bf16 v[170:173], v[194:197], v[206:209], v[170:173]
	s_and_b32 s22, s22, 0x3f00
	s_or_b32 s22, s22, s13
	s_lshl_b32 s23, s21, 23
	s_lshl_b32 s22, s22, 9
	v_mfma_f32_16x16x32_bf16 v[158:161], v[198:201], v[206:209], v[158:161]
	s_and_b32 s23, s23, 0x7000000
	s_or_b32 s22, s22, s23
	s_lshl_b32 s23, s21, 8
	s_and_b32 s23, s23, 0x100
	s_or_b32 s22, s22, s23
	s_or_b32 s23, s22, 0x4000
	buffer_load_dwordx4 v[10:13], v1, s[4:7], s22 offen sc0 nt
	v_mfma_f32_16x16x32_bf16 v[142:145], v[202:205], v[206:209], v[142:145]
	ds_read_b128 v[206:209], v238 offset:1024
	s_waitcnt lgkmcnt(10)
	v_mfma_f32_16x16x32_bf16 v[166:169], v[178:181], v[210:213], v[166:169]
	v_mfma_f32_16x16x32_bf16 v[162:165], v[194:197], v[210:213], v[162:165]
	v_mfma_f32_16x16x32_bf16 v[146:149], v[198:201], v[210:213], v[146:149]
	buffer_load_dwordx4 v[18:21], v1, s[4:7], s23 offen sc0 nt
	s_or_b32 s23, s22, 0x8000
	v_mfma_f32_16x16x32_bf16 v[122:125], v[202:205], v[210:213], v[122:125]
	ds_read_b128 v[210:213], v238 offset:3072
	s_waitcnt lgkmcnt(9)
	v_mfma_f32_16x16x32_bf16 v[154:157], v[178:181], v[214:217], v[154:157]
	v_mfma_f32_16x16x32_bf16 v[150:153], v[194:197], v[214:217], v[150:153]
	v_mfma_f32_16x16x32_bf16 v[130:133], v[198:201], v[214:217], v[130:133]
	buffer_load_dwordx4 v[22:25], v1, s[4:7], s23 offen sc0 nt
	s_or_b32 s23, s22, 0xc000
	v_mfma_f32_16x16x32_bf16 v[106:109], v[202:205], v[214:217], v[106:109]
	ds_read_b128 v[214:217], v238 offset:5120
	s_waitcnt lgkmcnt(8)
	v_mfma_f32_16x16x32_bf16 v[138:141], v[178:181], v[218:221], v[138:141]
	v_mfma_f32_16x16x32_bf16 v[134:137], v[194:197], v[218:221], v[134:137]
	v_mfma_f32_16x16x32_bf16 v[114:117], v[198:201], v[218:221], v[114:117]
	buffer_load_dwordx4 v[30:33], v1, s[4:7], s23 offen sc0 nt
	s_or_b32 s23, s22, 0x10000
	v_mfma_f32_16x16x32_bf16 v[90:93], v[202:205], v[218:221], v[90:93]
	ds_read_b128 v[218:221], v238 offset:7168
	s_waitcnt lgkmcnt(7)
	v_mfma_f32_16x16x32_bf16 v[126:129], v[178:181], v[222:225], v[126:129]
	v_mfma_f32_16x16x32_bf16 v[118:121], v[194:197], v[222:225], v[118:121]
	v_mfma_f32_16x16x32_bf16 v[98:101], v[198:201], v[222:225], v[98:101]
	buffer_load_dwordx4 v[34:37], v1, s[4:7], s23 offen sc0 nt
	s_or_b32 s23, s22, 0x14000
	v_mfma_f32_16x16x32_bf16 v[74:77], v[202:205], v[222:225], v[74:77]
	ds_read_b128 v[222:225], v238 offset:9216
	s_waitcnt lgkmcnt(6)
	v_mfma_f32_16x16x32_bf16 v[110:113], v[178:181], v[226:229], v[110:113]
	v_mfma_f32_16x16x32_bf16 v[102:105], v[194:197], v[226:229], v[102:105]
	v_mfma_f32_16x16x32_bf16 v[82:85], v[198:201], v[226:229], v[82:85]
	buffer_load_dwordx4 v[38:41], v1, s[4:7], s23 offen sc0 nt
	s_or_b32 s23, s22, 0x18000
	s_or_b32 s22, s22, 0x1c000
	v_mfma_f32_16x16x32_bf16 v[62:65], v[202:205], v[226:229], v[62:65]
	ds_read_b128 v[226:229], v238 offset:11264
	s_waitcnt lgkmcnt(5)
	v_mfma_f32_16x16x32_bf16 v[94:97], v[178:181], v[230:233], v[94:97]
	v_mfma_f32_16x16x32_bf16 v[86:89], v[194:197], v[230:233], v[86:89]
	v_mfma_f32_16x16x32_bf16 v[70:73], v[198:201], v[230:233], v[70:73]
	buffer_load_dwordx4 v[42:45], v1, s[4:7], s23 offen sc0 nt
	v_mfma_f32_16x16x32_bf16 v[54:57], v[202:205], v[230:233], v[54:57]
	s_waitcnt lgkmcnt(4)
	v_mfma_f32_16x16x32_bf16 v[78:81], v[178:181], v[234:237], v[78:81]
	v_mfma_f32_16x16x32_bf16 v[66:69], v[194:197], v[234:237], v[66:69]
	v_mfma_f32_16x16x32_bf16 v[58:61], v[198:201], v[234:237], v[58:61]
	buffer_load_dwordx4 v[46:49], v1, s[4:7], s22 offen sc0 nt
	v_mfma_f32_16x16x32_bf16 v[50:53], v[202:205], v[234:237], v[50:53]
	s_waitcnt lgkmcnt(0)
	s_barrier
	ds_read_b128 v[178:181], v182 offset:33792
	ds_read_b128 v[194:197], v182 offset:35840
	ds_read_b128 v[198:201], v182 offset:37888
	ds_read_b128 v[202:205], v182 offset:39936
	ds_read_b128 v[230:233], v238 offset:13312
	ds_read_b128 v[234:237], v238 offset:15360
	v_add_u32_e32 v182, s19, v190
	s_waitcnt vmcnt(11)
	ds_write_b128 v182, v[2:5] offset:32768
	s_waitcnt vmcnt(10)
	ds_write_b128 v182, v[6:9] offset:40960
	s_waitcnt vmcnt(9)
	ds_write_b128 v182, v[14:17] offset:49152
	s_waitcnt vmcnt(8)
	ds_write_b128 v182, v[26:29] offset:57344
	s_waitcnt lgkmcnt(0)
	s_barrier
	s_waitcnt lgkmcnt(11)
	v_mfma_f32_16x16x32_bf16 v[174:177], v[178:181], v[206:209], v[174:177]
	s_lshl_b32 s21, s21, 15
	s_and_b32 s21, s21, 0x78000
	s_or_b32 s21, s21, s14
	s_or_b32 s22, s21, 0x2000
	v_mfma_f32_16x16x32_bf16 v[170:173], v[194:197], v[206:209], v[170:173]
	v_mfma_f32_16x16x32_bf16 v[158:161], v[198:201], v[206:209], v[158:161]
	v_mfma_f32_16x16x32_bf16 v[142:145], v[202:205], v[206:209], v[142:145]
	s_waitcnt lgkmcnt(10)
	v_mfma_f32_16x16x32_bf16 v[166:169], v[178:181], v[210:213], v[166:169]
	v_mfma_f32_16x16x32_bf16 v[162:165], v[194:197], v[210:213], v[162:165]
	buffer_load_dwordx4 v[2:5], v188, s[0:3], s21 offen sc1
	v_mfma_f32_16x16x32_bf16 v[146:149], v[198:201], v[210:213], v[146:149]
	v_mfma_f32_16x16x32_bf16 v[122:125], v[202:205], v[210:213], v[122:125]
	s_waitcnt lgkmcnt(9)
	v_mfma_f32_16x16x32_bf16 v[154:157], v[178:181], v[214:217], v[154:157]
	v_mfma_f32_16x16x32_bf16 v[150:153], v[194:197], v[214:217], v[150:153]
	v_mfma_f32_16x16x32_bf16 v[130:133], v[198:201], v[214:217], v[130:133]
	v_mfma_f32_16x16x32_bf16 v[106:109], v[202:205], v[214:217], v[106:109]
	s_waitcnt lgkmcnt(8)
	v_mfma_f32_16x16x32_bf16 v[138:141], v[178:181], v[218:221], v[138:141]
	v_mfma_f32_16x16x32_bf16 v[134:137], v[194:197], v[218:221], v[134:137]
	buffer_load_dwordx4 v[6:9], v188, s[0:3], s22 offen sc1
	s_or_b32 s22, s21, 0x4000
	s_or_b32 s21, s21, 0x6000
	v_mfma_f32_16x16x32_bf16 v[114:117], v[198:201], v[218:221], v[114:117]
	v_mfma_f32_16x16x32_bf16 v[90:93], v[202:205], v[218:221], v[90:93]
	s_waitcnt lgkmcnt(7)
	v_mfma_f32_16x16x32_bf16 v[126:129], v[178:181], v[222:225], v[126:129]
	v_mfma_f32_16x16x32_bf16 v[118:121], v[194:197], v[222:225], v[118:121]
	v_mfma_f32_16x16x32_bf16 v[98:101], v[198:201], v[222:225], v[98:101]
	v_mfma_f32_16x16x32_bf16 v[74:77], v[202:205], v[222:225], v[74:77]
	s_waitcnt lgkmcnt(6)
	v_mfma_f32_16x16x32_bf16 v[110:113], v[178:181], v[226:229], v[110:113]
	v_mfma_f32_16x16x32_bf16 v[102:105], v[194:197], v[226:229], v[102:105]
	buffer_load_dwordx4 v[14:17], v188, s[0:3], s22 offen sc1
	v_mfma_f32_16x16x32_bf16 v[82:85], v[198:201], v[226:229], v[82:85]
	v_mfma_f32_16x16x32_bf16 v[62:65], v[202:205], v[226:229], v[62:65]
	s_waitcnt lgkmcnt(5)
	v_mfma_f32_16x16x32_bf16 v[94:97], v[178:181], v[230:233], v[94:97]
	v_mfma_f32_16x16x32_bf16 v[86:89], v[194:197], v[230:233], v[86:89]
	v_mfma_f32_16x16x32_bf16 v[70:73], v[198:201], v[230:233], v[70:73]
	v_mfma_f32_16x16x32_bf16 v[54:57], v[202:205], v[230:233], v[54:57]
	s_waitcnt lgkmcnt(4)
	v_mfma_f32_16x16x32_bf16 v[78:81], v[178:181], v[234:237], v[78:81]
	v_mfma_f32_16x16x32_bf16 v[66:69], v[194:197], v[234:237], v[66:69]
	buffer_load_dwordx4 v[26:29], v188, s[0:3], s21 offen sc1
	v_mfma_f32_16x16x32_bf16 v[58:61], v[198:201], v[234:237], v[58:61]
	v_mfma_f32_16x16x32_bf16 v[50:53], v[202:205], v[234:237], v[50:53]
	s_and_b32 s21, s20, 15
	s_cmp_lg_u32 s21, 15
	s_cbranch_scc1 .LBB1_3
	s_and_b32 s21, s18, 32
	s_add_i32 s21, s21, s12
	s_lshl_b32 s21, s21, 6
	s_and_b32 s21, s21, 0x3f00
	v_add_lshl_u32 v182, v193, s21, 9
	v_lshl_add_u64 v[206:207], v[184:185], 0, v[182:183]
	v_add_co_u32_e32 v208, vcc, s8, v206
	s_nop 1
	v_addc_co_u32_e32 v209, vcc, 0, v207, vcc
	v_add_co_u32_e32 v210, vcc, s15, v206
	s_nop 1
	v_addc_co_u32_e32 v211, vcc, 0, v207, vcc
	v_add_co_u32_e32 v212, vcc, s9, v206
	s_nop 1
	v_addc_co_u32_e32 v213, vcc, 0, v207, vcc
	v_add_co_u32_e32 v214, vcc, s16, v206
	s_nop 1
	v_addc_co_u32_e32 v215, vcc, 0, v207, vcc
	v_add_co_u32_e32 v216, vcc, s10, v206
	s_nop 1
	v_addc_co_u32_e32 v217, vcc, 0, v207, vcc
	v_add_co_u32_e32 v218, vcc, s17, v206
	s_nop 1
	v_addc_co_u32_e32 v219, vcc, 0, v207, vcc
	v_add_co_u32_e32 v220, vcc, s11, v206
	s_nop 1
	v_addc_co_u32_e32 v221, vcc, 0, v207, vcc
	global_store_dwordx4 v[206:207], v[174:177], off
	global_store_dwordx4 v[206:207], v[170:173], off offset:64
	global_store_dwordx4 v[206:207], v[158:161], off offset:128
	global_store_dwordx4 v[206:207], v[142:145], off offset:192
	global_store_dwordx4 v[208:209], v[166:169], off
	global_store_dwordx4 v[208:209], v[162:165], off offset:64
	global_store_dwordx4 v[208:209], v[146:149], off offset:128
	global_store_dwordx4 v[208:209], v[122:125], off offset:192
	global_store_dwordx4 v[210:211], v[154:157], off
	global_store_dwordx4 v[210:211], v[150:153], off offset:64
	global_store_dwordx4 v[210:211], v[130:133], off offset:128
	global_store_dwordx4 v[210:211], v[106:109], off offset:192
	global_store_dwordx4 v[212:213], v[138:141], off
	global_store_dwordx4 v[212:213], v[134:137], off offset:64
	global_store_dwordx4 v[212:213], v[114:117], off offset:128
	global_store_dwordx4 v[212:213], v[90:93], off offset:192
	global_store_dwordx4 v[214:215], v[126:129], off
	global_store_dwordx4 v[214:215], v[118:121], off offset:64
	global_store_dwordx4 v[214:215], v[98:101], off offset:128
	global_store_dwordx4 v[214:215], v[74:77], off offset:192
	global_store_dwordx4 v[216:217], v[110:113], off
	global_store_dwordx4 v[216:217], v[102:105], off offset:64
	global_store_dwordx4 v[216:217], v[82:85], off offset:128
	global_store_dwordx4 v[216:217], v[62:65], off offset:192
	global_store_dwordx4 v[218:219], v[94:97], off
	global_store_dwordx4 v[218:219], v[86:89], off offset:64
	global_store_dwordx4 v[218:219], v[70:73], off offset:128
	global_store_dwordx4 v[218:219], v[54:57], off offset:192
	global_store_dwordx4 v[220:221], v[78:81], off
	global_store_dwordx4 v[220:221], v[66:69], off offset:64
	global_store_dwordx4 v[220:221], v[58:61], off offset:128
	global_store_dwordx4 v[220:221], v[50:53], off offset:192
.Lpd_tail:
	s_waitcnt lgkmcnt(0)
	s_barrier
	s_add_i32 s20, s20, 1
	s_add_i32 s18, s18, 2
	v_add_u32_e32 v182, s19, v191
	v_add_u32_e32 v238, s19, v192
	ds_read_b128 v[178:181], v182 offset:32768
	ds_read_b128 v[194:197], v182 offset:34816
	ds_read_b128 v[198:201], v182 offset:36864
	ds_read_b128 v[202:205], v182 offset:38912
	ds_read_b128 v[206:209], v238
	ds_read_b128 v[210:213], v238 offset:2048
	ds_read_b128 v[214:217], v238 offset:4096
	ds_read_b128 v[218:221], v238 offset:6144
	ds_read_b128 v[222:225], v238 offset:8192
	ds_read_b128 v[226:229], v238 offset:10240
	ds_read_b128 v[230:233], v238 offset:12288
	ds_read_b128 v[234:237], v238 offset:14336
	s_min_u32 s21, s20, 29
	s_xor_b32 s19, s19, 0x10000
	v_add_u32_e32 v239, s19, v189
	s_waitcnt vmcnt(43)
	v_cvt_pk_bf16_f32 v13, v12, v13
	v_cvt_pk_bf16_f32 v12, v10, v11
	s_waitcnt vmcnt(42)
	v_cvt_pk_bf16_f32 v11, v20, v21
	v_cvt_pk_bf16_f32 v10, v18, v19
	ds_write2st64_b64 v239, v[12:13], v[10:11] offset1:8
	s_waitcnt vmcnt(41)
	v_cvt_pk_bf16_f32 v11, v24, v25
	v_cvt_pk_bf16_f32 v10, v22, v23
	s_waitcnt vmcnt(40)
	v_cvt_pk_bf16_f32 v13, v32, v33
	v_cvt_pk_bf16_f32 v12, v30, v31
	ds_write2st64_b64 v239, v[10:11], v[12:13] offset0:16 offset1:24
	s_waitcnt vmcnt(39)
	v_cvt_pk_bf16_f32 v11, v36, v37
	v_cvt_pk_bf16_f32 v10, v34, v35
	s_waitcnt vmcnt(38)
	v_cvt_pk_bf16_f32 v13, v40, v41
	v_cvt_pk_bf16_f32 v12, v38, v39
	ds_write2st64_b64 v239, v[10:11], v[12:13] offset0:32 offset1:40
	s_waitcnt vmcnt(37)
	v_cvt_pk_bf16_f32 v11, v44, v45
	v_cvt_pk_bf16_f32 v10, v42, v43
	s_waitcnt vmcnt(36)
	v_cvt_pk_bf16_f32 v13, v48, v49
	v_cvt_pk_bf16_f32 v12, v46, v47
	ds_write2st64_b64 v239, v[10:11], v[12:13] offset0:48 offset1:56
	s_waitcnt lgkmcnt(0)
	s_add_i32 s21, s21, 2
	s_barrier
	s_waitcnt lgkmcnt(11)
	v_mfma_f32_16x16x32_bf16 v[174:177], v[178:181], v[206:209], v[240:243]
	s_lshl_b32 s22, s21, 1
	s_and_b32 s22, s22, 0x60
	s_add_i32 s22, s22, s12
	s_lshl_b32 s22, s22, 6
	v_mfma_f32_16x16x32_bf16 v[170:173], v[194:197], v[206:209], v[244:247]
	s_and_b32 s22, s22, 0x3f00
	s_or_b32 s22, s22, s13
	s_lshl_b32 s23, s21, 23
	s_lshl_b32 s22, s22, 9
	v_mfma_f32_16x16x32_bf16 v[158:161], v[198:201], v[206:209], v[248:251]
	s_and_b32 s23, s23, 0x7000000
	s_or_b32 s22, s22, s23
	s_lshl_b32 s23, s21, 8
	s_and_b32 s23, s23, 0x100
	s_or_b32 s22, s22, s23
	s_or_b32 s23, s22, 0x4000
	buffer_load_dwordx4 v[10:13], v1, s[4:7], s22 offen sc0 nt
	v_mfma_f32_16x16x32_bf16 v[142:145], v[202:205], v[206:209], v[252:255]
	ds_read_b128 v[206:209], v238 offset:1024
	s_waitcnt lgkmcnt(10)
	v_mfma_f32_16x16x32_bf16 v[166:169], v[178:181], v[210:213], v[240:243]
	v_mfma_f32_16x16x32_bf16 v[162:165], v[194:197], v[210:213], v[244:247]
	v_mfma_f32_16x16x32_bf16 v[146:149], v[198:201], v[210:213], v[248:251]
	buffer_load_dwordx4 v[18:21], v1, s[4:7], s23 offen sc0 nt
	s_or_b32 s23, s22, 0x8000
	v_mfma_f32_16x16x32_bf16 v[122:125], v[202:205], v[210:213], v[252:255]
	ds_read_b128 v[210:213], v238 offset:3072
	s_waitcnt lgkmcnt(9)
	v_mfma_f32_16x16x32_bf16 v[154:157], v[178:181], v[214:217], v[240:243]
	v_mfma_f32_16x16x32_bf16 v[150:153], v[194:197], v[214:217], v[244:247]
	v_mfma_f32_16x16x32_bf16 v[130:133], v[198:201], v[214:217], v[248:251]
	buffer_load_dwordx4 v[22:25], v1, s[4:7], s23 offen sc0 nt
	s_or_b32 s23, s22, 0xc000
	v_mfma_f32_16x16x32_bf16 v[106:109], v[202:205], v[214:217], v[252:255]
	ds_read_b128 v[214:217], v238 offset:5120
	s_waitcnt lgkmcnt(8)
	v_mfma_f32_16x16x32_bf16 v[138:141], v[178:181], v[218:221], v[240:243]
	v_mfma_f32_16x16x32_bf16 v[134:137], v[194:197], v[218:221], v[244:247]
	v_mfma_f32_16x16x32_bf16 v[114:117], v[198:201], v[218:221], v[248:251]
	buffer_load_dwordx4 v[30:33], v1, s[4:7], s23 offen sc0 nt
	s_or_b32 s23, s22, 0x10000
	v_mfma_f32_16x16x32_bf16 v[90:93], v[202:205], v[218:221], v[252:255]
	ds_read_b128 v[218:221], v238 offset:7168
	s_waitcnt lgkmcnt(7)
	v_mfma_f32_16x16x32_bf16 v[126:129], v[178:181], v[222:225], v[240:243]
	v_mfma_f32_16x16x32_bf16 v[118:121], v[194:197], v[222:225], v[244:247]
	v_mfma_f32_16x16x32_bf16 v[98:101], v[198:201], v[222:225], v[248:251]
	buffer_load_dwordx4 v[34:37], v1, s[4:7], s23 offen sc0 nt
	s_or_b32 s23, s22, 0x14000
	v_mfma_f32_16x16x32_bf16 v[74:77], v[202:205], v[222:225], v[252:255]
	ds_read_b128 v[222:225], v238 offset:9216
	s_waitcnt lgkmcnt(6)
	v_mfma_f32_16x16x32_bf16 v[110:113], v[178:181], v[226:229], v[240:243]
	v_mfma_f32_16x16x32_bf16 v[102:105], v[194:197], v[226:229], v[244:247]
	v_mfma_f32_16x16x32_bf16 v[82:85], v[198:201], v[226:229], v[248:251]
	buffer_load_dwordx4 v[38:41], v1, s[4:7], s23 offen sc0 nt
	s_or_b32 s23, s22, 0x18000
	s_or_b32 s22, s22, 0x1c000
	v_mfma_f32_16x16x32_bf16 v[62:65], v[202:205], v[226:229], v[252:255]
	ds_read_b128 v[226:229], v238 offset:11264
	s_waitcnt lgkmcnt(5)
	v_mfma_f32_16x16x32_bf16 v[94:97], v[178:181], v[230:233], v[240:243]
	v_mfma_f32_16x16x32_bf16 v[86:89], v[194:197], v[230:233], v[244:247]
	v_mfma_f32_16x16x32_bf16 v[70:73], v[198:201], v[230:233], v[248:251]
	buffer_load_dwordx4 v[42:45], v1, s[4:7], s23 offen sc0 nt
	v_mfma_f32_16x16x32_bf16 v[54:57], v[202:205], v[230:233], v[252:255]
	s_waitcnt lgkmcnt(4)
	v_mfma_f32_16x16x32_bf16 v[78:81], v[178:181], v[234:237], v[240:243]
	v_mfma_f32_16x16x32_bf16 v[66:69], v[194:197], v[234:237], v[244:247]
	v_mfma_f32_16x16x32_bf16 v[58:61], v[198:201], v[234:237], v[248:251]
	buffer_load_dwordx4 v[46:49], v1, s[4:7], s22 offen sc0 nt
	v_mfma_f32_16x16x32_bf16 v[50:53], v[202:205], v[234:237], v[252:255]
	s_waitcnt lgkmcnt(0)
	s_barrier
	ds_read_b128 v[178:181], v182 offset:33792
	ds_read_b128 v[194:197], v182 offset:35840
	ds_read_b128 v[198:201], v182 offset:37888
	ds_read_b128 v[202:205], v182 offset:39936
	ds_read_b128 v[230:233], v238 offset:13312
	ds_read_b128 v[234:237], v238 offset:15360
	v_add_u32_e32 v182, s19, v190
	s_waitcnt vmcnt(43)
	ds_write_b128 v182, v[2:5] offset:32768
	s_waitcnt vmcnt(42)
	ds_write_b128 v182, v[6:9] offset:40960
	s_waitcnt vmcnt(41)
	ds_write_b128 v182, v[14:17] offset:49152
	s_waitcnt vmcnt(40)
	ds_write_b128 v182, v[26:29] offset:57344
	s_waitcnt lgkmcnt(0)
	s_barrier
	s_waitcnt lgkmcnt(11)
	v_mfma_f32_16x16x32_bf16 v[174:177], v[178:181], v[206:209], v[174:177]
	s_lshl_b32 s21, s21, 15
	s_and_b32 s21, s21, 0x78000
	s_or_b32 s21, s21, s14
	s_or_b32 s22, s21, 0x2000
	v_mfma_f32_16x16x32_bf16 v[170:173], v[194:197], v[206:209], v[170:173]
	v_mfma_f32_16x16x32_bf16 v[158:161], v[198:201], v[206:209], v[158:161]
	v_mfma_f32_16x16x32_bf16 v[142:145], v[202:205], v[206:209], v[142:145]
	s_waitcnt lgkmcnt(10)
	v_mfma_f32_16x16x32_bf16 v[166:169], v[178:181], v[210:213], v[166:169]
	v_mfma_f32_16x16x32_bf16 v[162:165], v[194:197], v[210:213], v[162:165]
	buffer_load_dwordx4 v[2:5], v188, s[0:3], s21 offen sc1
	v_mfma_f32_16x16x32_bf16 v[146:149], v[198:201], v[210:213], v[146:149]
	v_mfma_f32_16x16x32_bf16 v[122:125], v[202:205], v[210:213], v[122:125]
	s_waitcnt lgkmcnt(9)
	v_mfma_f32_16x16x32_bf16 v[154:157], v[178:181], v[214:217], v[154:157]
	v_mfma_f32_16x16x32_bf16 v[150:153], v[194:197], v[214:217], v[150:153]
	v_mfma_f32_16x16x32_bf16 v[130:133], v[198:201], v[214:217], v[130:133]
	v_mfma_f32_16x16x32_bf16 v[106:109], v[202:205], v[214:217], v[106:109]
	s_waitcnt lgkmcnt(8)
	v_mfma_f32_16x16x32_bf16 v[138:141], v[178:181], v[218:221], v[138:141]
	v_mfma_f32_16x16x32_bf16 v[134:137], v[194:197], v[218:221], v[134:137]
	buffer_load_dwordx4 v[6:9], v188, s[0:3], s22 offen sc1
	s_or_b32 s22, s21, 0x4000
	s_or_b32 s21, s21, 0x6000
	v_mfma_f32_16x16x32_bf16 v[114:117], v[198:201], v[218:221], v[114:117]
	v_mfma_f32_16x16x32_bf16 v[90:93], v[202:205], v[218:221], v[90:93]
	s_waitcnt lgkmcnt(7)
	v_mfma_f32_16x16x32_bf16 v[126:129], v[178:181], v[222:225], v[126:129]
	v_mfma_f32_16x16x32_bf16 v[118:121], v[194:197], v[222:225], v[118:121]
	v_mfma_f32_16x16x32_bf16 v[98:101], v[198:201], v[222:225], v[98:101]
	v_mfma_f32_16x16x32_bf16 v[74:77], v[202:205], v[222:225], v[74:77]
	s_waitcnt lgkmcnt(6)
	v_mfma_f32_16x16x32_bf16 v[110:113], v[178:181], v[226:229], v[110:113]
	v_mfma_f32_16x16x32_bf16 v[102:105], v[194:197], v[226:229], v[102:105]
	buffer_load_dwordx4 v[14:17], v188, s[0:3], s22 offen sc1
	v_mfma_f32_16x16x32_bf16 v[82:85], v[198:201], v[226:229], v[82:85]
	v_mfma_f32_16x16x32_bf16 v[62:65], v[202:205], v[226:229], v[62:65]
	s_waitcnt lgkmcnt(5)
	v_mfma_f32_16x16x32_bf16 v[94:97], v[178:181], v[230:233], v[94:97]
	v_mfma_f32_16x16x32_bf16 v[86:89], v[194:197], v[230:233], v[86:89]
	v_mfma_f32_16x16x32_bf16 v[70:73], v[198:201], v[230:233], v[70:73]
	v_mfma_f32_16x16x32_bf16 v[54:57], v[202:205], v[230:233], v[54:57]
	s_waitcnt lgkmcnt(4)
	v_mfma_f32_16x16x32_bf16 v[78:81], v[178:181], v[234:237], v[78:81]
	v_mfma_f32_16x16x32_bf16 v[66:69], v[194:197], v[234:237], v[66:69]
	buffer_load_dwordx4 v[26:29], v188, s[0:3], s21 offen sc1
	v_mfma_f32_16x16x32_bf16 v[58:61], v[198:201], v[234:237], v[58:61]
	v_mfma_f32_16x16x32_bf16 v[50:53], v[202:205], v[234:237], v[50:53]
	s_branch .LBB1_3
.Lt30:
	v_add_u32_e32 v182, s19, v191
	v_add_u32_e32 v238, s19, v192
	ds_read_b128 v[178:181], v182 offset:32768
	ds_read_b128 v[194:197], v182 offset:34816
	ds_read_b128 v[198:201], v182 offset:36864
	ds_read_b128 v[202:205], v182 offset:38912
	ds_read_b128 v[206:209], v238
	ds_read_b128 v[210:213], v238 offset:2048
	ds_read_b128 v[214:217], v238 offset:4096
	ds_read_b128 v[218:221], v238 offset:6144
	ds_read_b128 v[222:225], v238 offset:8192
	ds_read_b128 v[226:229], v238 offset:10240
	ds_read_b128 v[230:233], v238 offset:12288
	ds_read_b128 v[234:237], v238 offset:14336
	s_min_u32 s21, s20, 29
	s_xor_b32 s19, s19, 0x10000
	v_add_u32_e32 v239, s19, v189
	s_waitcnt vmcnt(11)
	v_cvt_pk_bf16_f32 v13, v12, v13
	v_cvt_pk_bf16_f32 v12, v10, v11
	s_waitcnt vmcnt(10)
	v_cvt_pk_bf16_f32 v11, v20, v21
	v_cvt_pk_bf16_f32 v10, v18, v19
	ds_write2st64_b64 v239, v[12:13], v[10:11] offset1:8
	s_waitcnt vmcnt(9)
	v_cvt_pk_bf16_f32 v11, v24, v25
	v_cvt_pk_bf16_f32 v10, v22, v23
	s_waitcnt vmcnt(8)
	v_cvt_pk_bf16_f32 v13, v32, v33
	v_cvt_pk_bf16_f32 v12, v30, v31
	ds_write2st64_b64 v239, v[10:11], v[12:13] offset0:16 offset1:24
	s_waitcnt vmcnt(7)
	v_cvt_pk_bf16_f32 v11, v36, v37
	v_cvt_pk_bf16_f32 v10, v34, v35
	s_waitcnt vmcnt(6)
	v_cvt_pk_bf16_f32 v13, v40, v41
	v_cvt_pk_bf16_f32 v12, v38, v39
	ds_write2st64_b64 v239, v[10:11], v[12:13] offset0:32 offset1:40
	s_waitcnt vmcnt(5)
	v_cvt_pk_bf16_f32 v11, v44, v45
	v_cvt_pk_bf16_f32 v10, v42, v43
	s_waitcnt vmcnt(4)
	v_cvt_pk_bf16_f32 v13, v48, v49
	v_cvt_pk_bf16_f32 v12, v46, v47
	ds_write2st64_b64 v239, v[10:11], v[12:13] offset0:48 offset1:56
	s_waitcnt lgkmcnt(0)
	s_add_i32 s21, s21, 2
	s_barrier
	s_waitcnt lgkmcnt(11)
	v_mfma_f32_16x16x32_bf16 v[174:177], v[178:181], v[206:209], v[174:177]
	s_lshl_b32 s22, s21, 1
	s_and_b32 s22, s22, 0x60
	s_add_i32 s22, s22, s12
	s_lshl_b32 s22, s22, 6
	v_mfma_f32_16x16x32_bf16 v[170:173], v[194:197], v[206:209], v[170:173]
	s_and_b32 s22, s22, 0x3f00
	s_or_b32 s22, s22, s13
	s_lshl_b32 s23, s21, 23
	s_lshl_b32 s22, s22, 9
	v_mfma_f32_16x16x32_bf16 v[158:161], v[198:201], v[206:209], v[158:161]
	s_and_b32 s23, s23, 0x7000000
	s_or_b32 s22, s22, s23
	s_lshl_b32 s23, s21, 8
	s_and_b32 s23, s23, 0x100
	s_or_b32 s22, s22, s23
	s_or_b32 s23, s22, 0x4000
	v_mfma_f32_16x16x32_bf16 v[142:145], v[202:205], v[206:209], v[142:145]
	ds_read_b128 v[206:209], v238 offset:1024
	s_waitcnt lgkmcnt(10)
	v_mfma_f32_16x16x32_bf16 v[166:169], v[178:181], v[210:213], v[166:169]
	v_mfma_f32_16x16x32_bf16 v[162:165], v[194:197], v[210:213], v[162:165]
	v_mfma_f32_16x16x32_bf16 v[146:149], v[198:201], v[210:213], v[146:149]
	s_or_b32 s23, s22, 0x8000
	v_mfma_f32_16x16x32_bf16 v[122:125], v[202:205], v[210:213], v[122:125]
	ds_read_b128 v[210:213], v238 offset:3072
	s_waitcnt lgkmcnt(9)
	v_mfma_f32_16x16x32_bf16 v[154:157], v[178:181], v[214:217], v[154:157]
	v_mfma_f32_16x16x32_bf16 v[150:153], v[194:197], v[214:217], v[150:153]
	v_mfma_f32_16x16x32_bf16 v[130:133], v[198:201], v[214:217], v[130:133]
	s_or_b32 s23, s22, 0xc000
	v_mfma_f32_16x16x32_bf16 v[106:109], v[202:205], v[214:217], v[106:109]
	ds_read_b128 v[214:217], v238 offset:5120
	s_waitcnt lgkmcnt(8)
	v_mfma_f32_16x16x32_bf16 v[138:141], v[178:181], v[218:221], v[138:141]
	v_mfma_f32_16x16x32_bf16 v[134:137], v[194:197], v[218:221], v[134:137]
	v_mfma_f32_16x16x32_bf16 v[114:117], v[198:201], v[218:221], v[114:117]
	s_or_b32 s23, s22, 0x10000
	v_mfma_f32_16x16x32_bf16 v[90:93], v[202:205], v[218:221], v[90:93]
	ds_read_b128 v[218:221], v238 offset:7168
	s_waitcnt lgkmcnt(7)
	v_mfma_f32_16x16x32_bf16 v[126:129], v[178:181], v[222:225], v[126:129]
	v_mfma_f32_16x16x32_bf16 v[118:121], v[194:197], v[222:225], v[118:121]
	v_mfma_f32_16x16x32_bf16 v[98:101], v[198:201], v[222:225], v[98:101]
	s_or_b32 s23, s22, 0x14000
	v_mfma_f32_16x16x32_bf16 v[74:77], v[202:205], v[222:225], v[74:77]
	ds_read_b128 v[222:225], v238 offset:9216
	s_waitcnt lgkmcnt(6)
	v_mfma_f32_16x16x32_bf16 v[110:113], v[178:181], v[226:229], v[110:113]
	v_mfma_f32_16x16x32_bf16 v[102:105], v[194:197], v[226:229], v[102:105]
	v_mfma_f32_16x16x32_bf16 v[82:85], v[198:201], v[226:229], v[82:85]
	s_or_b32 s23, s22, 0x18000
	s_or_b32 s22, s22, 0x1c000
	v_mfma_f32_16x16x32_bf16 v[62:65], v[202:205], v[226:229], v[62:65]
	ds_read_b128 v[226:229], v238 offset:11264
	s_waitcnt lgkmcnt(5)
	v_mfma_f32_16x16x32_bf16 v[94:97], v[178:181], v[230:233], v[94:97]
	v_mfma_f32_16x16x32_bf16 v[86:89], v[194:197], v[230:233], v[86:89]
	v_mfma_f32_16x16x32_bf16 v[70:73], v[198:201], v[230:233], v[70:73]
	v_mfma_f32_16x16x32_bf16 v[54:57], v[202:205], v[230:233], v[54:57]
	s_waitcnt lgkmcnt(4)
	v_mfma_f32_16x16x32_bf16 v[78:81], v[178:181], v[234:237], v[78:81]
	v_mfma_f32_16x16x32_bf16 v[66:69], v[194:197], v[234:237], v[66:69]
	v_mfma_f32_16x16x32_bf16 v[58:61], v[198:201], v[234:237], v[58:61]
	v_mfma_f32_16x16x32_bf16 v[50:53], v[202:205], v[234:237], v[50:53]
	s_waitcnt lgkmcnt(0)
	s_barrier
	ds_read_b128 v[178:181], v182 offset:33792
	ds_read_b128 v[194:197], v182 offset:35840
	ds_read_b128 v[198:201], v182 offset:37888
	ds_read_b128 v[202:205], v182 offset:39936
	ds_read_b128 v[230:233], v238 offset:13312
	ds_read_b128 v[234:237], v238 offset:15360
	v_add_u32_e32 v182, s19, v190
	s_waitcnt vmcnt(3)
	ds_write_b128 v182, v[2:5] offset:32768
	s_waitcnt vmcnt(2)
	ds_write_b128 v182, v[6:9] offset:40960
	s_waitcnt vmcnt(1)
	ds_write_b128 v182, v[14:17] offset:49152
	s_waitcnt vmcnt(0)
	ds_write_b128 v182, v[26:29] offset:57344
	s_waitcnt lgkmcnt(0)
	s_barrier
	s_waitcnt lgkmcnt(11)
	v_mfma_f32_16x16x32_bf16 v[174:177], v[178:181], v[206:209], v[174:177]
	s_lshl_b32 s21, s21, 15
	s_and_b32 s21, s21, 0x78000
	s_or_b32 s21, s21, s14
	s_or_b32 s22, s21, 0x2000
	v_mfma_f32_16x16x32_bf16 v[170:173], v[194:197], v[206:209], v[170:173]
	v_mfma_f32_16x16x32_bf16 v[158:161], v[198:201], v[206:209], v[158:161]
	v_mfma_f32_16x16x32_bf16 v[142:145], v[202:205], v[206:209], v[142:145]
	s_waitcnt lgkmcnt(10)
	v_mfma_f32_16x16x32_bf16 v[166:169], v[178:181], v[210:213], v[166:169]
	v_mfma_f32_16x16x32_bf16 v[162:165], v[194:197], v[210:213], v[162:165]
	v_mfma_f32_16x16x32_bf16 v[146:149], v[198:201], v[210:213], v[146:149]
	v_mfma_f32_16x16x32_bf16 v[122:125], v[202:205], v[210:213], v[122:125]
	s_waitcnt lgkmcnt(9)
	v_mfma_f32_16x16x32_bf16 v[154:157], v[178:181], v[214:217], v[154:157]
	v_mfma_f32_16x16x32_bf16 v[150:153], v[194:197], v[214:217], v[150:153]
	v_mfma_f32_16x16x32_bf16 v[130:133], v[198:201], v[214:217], v[130:133]
	v_mfma_f32_16x16x32_bf16 v[106:109], v[202:205], v[214:217], v[106:109]
	s_waitcnt lgkmcnt(8)
	v_mfma_f32_16x16x32_bf16 v[138:141], v[178:181], v[218:221], v[138:141]
	v_mfma_f32_16x16x32_bf16 v[134:137], v[194:197], v[218:221], v[134:137]
	s_or_b32 s22, s21, 0x4000
	s_or_b32 s21, s21, 0x6000
	v_mfma_f32_16x16x32_bf16 v[114:117], v[198:201], v[218:221], v[114:117]
	v_mfma_f32_16x16x32_bf16 v[90:93], v[202:205], v[218:221], v[90:93]
	s_waitcnt lgkmcnt(7)
	v_mfma_f32_16x16x32_bf16 v[126:129], v[178:181], v[222:225], v[126:129]
	v_mfma_f32_16x16x32_bf16 v[118:121], v[194:197], v[222:225], v[118:121]
	v_mfma_f32_16x16x32_bf16 v[98:101], v[198:201], v[222:225], v[98:101]
	v_mfma_f32_16x16x32_bf16 v[74:77], v[202:205], v[222:225], v[74:77]
	s_waitcnt lgkmcnt(6)
	v_mfma_f32_16x16x32_bf16 v[110:113], v[178:181], v[226:229], v[110:113]
	v_mfma_f32_16x16x32_bf16 v[102:105], v[194:197], v[226:229], v[102:105]
	v_mfma_f32_16x16x32_bf16 v[82:85], v[198:201], v[226:229], v[82:85]
	v_mfma_f32_16x16x32_bf16 v[62:65], v[202:205], v[226:229], v[62:65]
	s_waitcnt lgkmcnt(5)
	v_mfma_f32_16x16x32_bf16 v[94:97], v[178:181], v[230:233], v[94:97]
	v_mfma_f32_16x16x32_bf16 v[86:89], v[194:197], v[230:233], v[86:89]
	v_mfma_f32_16x16x32_bf16 v[70:73], v[198:201], v[230:233], v[70:73]
	v_mfma_f32_16x16x32_bf16 v[54:57], v[202:205], v[230:233], v[54:57]
	s_waitcnt lgkmcnt(4)
	v_mfma_f32_16x16x32_bf16 v[78:81], v[178:181], v[234:237], v[78:81]
	v_mfma_f32_16x16x32_bf16 v[66:69], v[194:197], v[234:237], v[66:69]
	v_mfma_f32_16x16x32_bf16 v[58:61], v[198:201], v[234:237], v[58:61]
	v_mfma_f32_16x16x32_bf16 v[50:53], v[202:205], v[234:237], v[50:53]
	s_waitcnt lgkmcnt(0)
	s_barrier
	s_add_i32 s20, s20, 1
	s_add_i32 s18, s18, 2
	v_add_u32_e32 v182, s19, v191
	v_add_u32_e32 v238, s19, v192
	ds_read_b128 v[178:181], v182 offset:32768
	ds_read_b128 v[194:197], v182 offset:34816
	ds_read_b128 v[198:201], v182 offset:36864
	ds_read_b128 v[202:205], v182 offset:38912
	ds_read_b128 v[206:209], v238
	ds_read_b128 v[210:213], v238 offset:2048
	ds_read_b128 v[214:217], v238 offset:4096
	ds_read_b128 v[218:221], v238 offset:6144
	ds_read_b128 v[222:225], v238 offset:8192
	ds_read_b128 v[226:229], v238 offset:10240
	ds_read_b128 v[230:233], v238 offset:12288
	ds_read_b128 v[234:237], v238 offset:14336
	s_min_u32 s21, s20, 29
	s_xor_b32 s19, s19, 0x10000
	v_add_u32_e32 v239, s19, v189
	s_waitcnt lgkmcnt(0)
	s_add_i32 s21, s21, 2
	s_barrier
	s_waitcnt lgkmcnt(11)
	v_mfma_f32_16x16x32_bf16 v[174:177], v[178:181], v[206:209], v[174:177]
	s_lshl_b32 s22, s21, 1
	s_and_b32 s22, s22, 0x60
	s_add_i32 s22, s22, s12
	s_lshl_b32 s22, s22, 6
	v_mfma_f32_16x16x32_bf16 v[170:173], v[194:197], v[206:209], v[170:173]
	s_and_b32 s22, s22, 0x3f00
	s_or_b32 s22, s22, s13
	s_lshl_b32 s23, s21, 23
	s_lshl_b32 s22, s22, 9
	v_mfma_f32_16x16x32_bf16 v[158:161], v[198:201], v[206:209], v[158:161]
	s_and_b32 s23, s23, 0x7000000
	s_or_b32 s22, s22, s23
	s_lshl_b32 s23, s21, 8
	s_and_b32 s23, s23, 0x100
	s_or_b32 s22, s22, s23
	s_or_b32 s23, s22, 0x4000
	v_mfma_f32_16x16x32_bf16 v[142:145], v[202:205], v[206:209], v[142:145]
	ds_read_b128 v[206:209], v238 offset:1024
	s_waitcnt lgkmcnt(10)
	v_mfma_f32_16x16x32_bf16 v[166:169], v[178:181], v[210:213], v[166:169]
	v_mfma_f32_16x16x32_bf16 v[162:165], v[194:197], v[210:213], v[162:165]
	v_mfma_f32_16x16x32_bf16 v[146:149], v[198:201], v[210:213], v[146:149]
	s_or_b32 s23, s22, 0x8000
	v_mfma_f32_16x16x32_bf16 v[122:125], v[202:205], v[210:213], v[122:125]
	ds_read_b128 v[210:213], v238 offset:3072
	s_waitcnt lgkmcnt(9)
	v_mfma_f32_16x16x32_bf16 v[154:157], v[178:181], v[214:217], v[154:157]
	v_mfma_f32_16x16x32_bf16 v[150:153], v[194:197], v[214:217], v[150:153]
	v_mfma_f32_16x16x32_bf16 v[130:133], v[198:201], v[214:217], v[130:133]
	s_or_b32 s23, s22, 0xc000
	v_mfma_f32_16x16x32_bf16 v[106:109], v[202:205], v[214:217], v[106:109]
	ds_read_b128 v[214:217], v238 offset:5120
	s_waitcnt lgkmcnt(8)
	v_mfma_f32_16x16x32_bf16 v[138:141], v[178:181], v[218:221], v[138:141]
	v_mfma_f32_16x16x32_bf16 v[134:137], v[194:197], v[218:221], v[134:137]
	v_mfma_f32_16x16x32_bf16 v[114:117], v[198:201], v[218:221], v[114:117]
	s_or_b32 s23, s22, 0x10000
	v_mfma_f32_16x16x32_bf16 v[90:93], v[202:205], v[218:221], v[90:93]
	ds_read_b128 v[218:221], v238 offset:7168
	s_waitcnt lgkmcnt(7)
	v_mfma_f32_16x16x32_bf16 v[126:129], v[178:181], v[222:225], v[126:129]
	v_mfma_f32_16x16x32_bf16 v[118:121], v[194:197], v[222:225], v[118:121]
	v_mfma_f32_16x16x32_bf16 v[98:101], v[198:201], v[222:225], v[98:101]
	s_or_b32 s23, s22, 0x14000
	v_mfma_f32_16x16x32_bf16 v[74:77], v[202:205], v[222:225], v[74:77]
	ds_read_b128 v[222:225], v238 offset:9216
	s_waitcnt lgkmcnt(6)
	v_mfma_f32_16x16x32_bf16 v[110:113], v[178:181], v[226:229], v[110:113]
	v_mfma_f32_16x16x32_bf16 v[102:105], v[194:197], v[226:229], v[102:105]
	v_mfma_f32_16x16x32_bf16 v[82:85], v[198:201], v[226:229], v[82:85]
	s_or_b32 s23, s22, 0x18000
	s_or_b32 s22, s22, 0x1c000
	v_mfma_f32_16x16x32_bf16 v[62:65], v[202:205], v[226:229], v[62:65]
	ds_read_b128 v[226:229], v238 offset:11264
	s_waitcnt lgkmcnt(5)
	v_mfma_f32_16x16x32_bf16 v[94:97], v[178:181], v[230:233], v[94:97]
	v_mfma_f32_16x16x32_bf16 v[86:89], v[194:197], v[230:233], v[86:89]
	v_mfma_f32_16x16x32_bf16 v[70:73], v[198:201], v[230:233], v[70:73]
	v_mfma_f32_16x16x32_bf16 v[54:57], v[202:205], v[230:233], v[54:57]
	s_waitcnt lgkmcnt(4)
	v_mfma_f32_16x16x32_bf16 v[78:81], v[178:181], v[234:237], v[78:81]
	v_mfma_f32_16x16x32_bf16 v[66:69], v[194:197], v[234:237], v[66:69]
	v_mfma_f32_16x16x32_bf16 v[58:61], v[198:201], v[234:237], v[58:61]
	v_mfma_f32_16x16x32_bf16 v[50:53], v[202:205], v[234:237], v[50:53]
	s_waitcnt lgkmcnt(0)
	s_barrier
	ds_read_b128 v[178:181], v182 offset:33792
	ds_read_b128 v[194:197], v182 offset:35840
	ds_read_b128 v[198:201], v182 offset:37888
	ds_read_b128 v[202:205], v182 offset:39936
	ds_read_b128 v[230:233], v238 offset:13312
	ds_read_b128 v[234:237], v238 offset:15360
	s_waitcnt lgkmcnt(0)
	s_barrier
	s_waitcnt lgkmcnt(11)
	v_mfma_f32_16x16x32_bf16 v[174:177], v[178:181], v[206:209], v[174:177]
	s_lshl_b32 s21, s21, 15
	s_and_b32 s21, s21, 0x78000
	s_or_b32 s21, s21, s14
	s_or_b32 s22, s21, 0x2000
	v_mfma_f32_16x16x32_bf16 v[170:173], v[194:197], v[206:209], v[170:173]
	v_mfma_f32_16x16x32_bf16 v[158:161], v[198:201], v[206:209], v[158:161]
	v_mfma_f32_16x16x32_bf16 v[142:145], v[202:205], v[206:209], v[142:145]
	s_waitcnt lgkmcnt(10)
	v_mfma_f32_16x16x32_bf16 v[166:169], v[178:181], v[210:213], v[166:169]
	v_mfma_f32_16x16x32_bf16 v[162:165], v[194:197], v[210:213], v[162:165]
	v_mfma_f32_16x16x32_bf16 v[146:149], v[198:201], v[210:213], v[146:149]
	v_mfma_f32_16x16x32_bf16 v[122:125], v[202:205], v[210:213], v[122:125]
	s_waitcnt lgkmcnt(9)
	v_mfma_f32_16x16x32_bf16 v[154:157], v[178:181], v[214:217], v[154:157]
	v_mfma_f32_16x16x32_bf16 v[150:153], v[194:197], v[214:217], v[150:153]
	v_mfma_f32_16x16x32_bf16 v[130:133], v[198:201], v[214:217], v[130:133]
	v_mfma_f32_16x16x32_bf16 v[106:109], v[202:205], v[214:217], v[106:109]
	s_waitcnt lgkmcnt(8)
	v_mfma_f32_16x16x32_bf16 v[138:141], v[178:181], v[218:221], v[138:141]
	v_mfma_f32_16x16x32_bf16 v[134:137], v[194:197], v[218:221], v[134:137]
	s_or_b32 s22, s21, 0x4000
	s_or_b32 s21, s21, 0x6000
	v_mfma_f32_16x16x32_bf16 v[114:117], v[198:201], v[218:221], v[114:117]
	v_mfma_f32_16x16x32_bf16 v[90:93], v[202:205], v[218:221], v[90:93]
	s_waitcnt lgkmcnt(7)
	v_mfma_f32_16x16x32_bf16 v[126:129], v[178:181], v[222:225], v[126:129]
	v_mfma_f32_16x16x32_bf16 v[118:121], v[194:197], v[222:225], v[118:121]
	v_mfma_f32_16x16x32_bf16 v[98:101], v[198:201], v[222:225], v[98:101]
	v_mfma_f32_16x16x32_bf16 v[74:77], v[202:205], v[222:225], v[74:77]
	s_waitcnt lgkmcnt(6)
	v_mfma_f32_16x16x32_bf16 v[110:113], v[178:181], v[226:229], v[110:113]
	v_mfma_f32_16x16x32_bf16 v[102:105], v[194:197], v[226:229], v[102:105]
	v_mfma_f32_16x16x32_bf16 v[82:85], v[198:201], v[226:229], v[82:85]
	v_mfma_f32_16x16x32_bf16 v[62:65], v[202:205], v[226:229], v[62:65]
	s_waitcnt lgkmcnt(5)
	v_mfma_f32_16x16x32_bf16 v[94:97], v[178:181], v[230:233], v[94:97]
	v_mfma_f32_16x16x32_bf16 v[86:89], v[194:197], v[230:233], v[86:89]
	v_mfma_f32_16x16x32_bf16 v[70:73], v[198:201], v[230:233], v[70:73]
	v_mfma_f32_16x16x32_bf16 v[54:57], v[202:205], v[230:233], v[54:57]
	s_waitcnt lgkmcnt(4)
	v_mfma_f32_16x16x32_bf16 v[78:81], v[178:181], v[234:237], v[78:81]
	v_mfma_f32_16x16x32_bf16 v[66:69], v[194:197], v[234:237], v[66:69]
	v_mfma_f32_16x16x32_bf16 v[58:61], v[198:201], v[234:237], v[58:61]
	v_mfma_f32_16x16x32_bf16 v[50:53], v[202:205], v[234:237], v[50:53]
	s_and_b32 s21, s18, 32
	s_add_i32 s21, s21, s12
	s_lshl_b32 s21, s21, 6
	s_and_b32 s21, s21, 0x3f00
	v_add_lshl_u32 v182, v193, s21, 9
	v_lshl_add_u64 v[206:207], v[184:185], 0, v[182:183]
	v_add_co_u32_e32 v208, vcc, s8, v206
	s_nop 1
	v_addc_co_u32_e32 v209, vcc, 0, v207, vcc
	v_add_co_u32_e32 v210, vcc, s15, v206
	s_nop 1
	v_addc_co_u32_e32 v211, vcc, 0, v207, vcc
	v_add_co_u32_e32 v212, vcc, s9, v206
	s_nop 1
	v_addc_co_u32_e32 v213, vcc, 0, v207, vcc
	v_add_co_u32_e32 v214, vcc, s16, v206
	s_nop 1
	v_addc_co_u32_e32 v215, vcc, 0, v207, vcc
	v_add_co_u32_e32 v216, vcc, s10, v206
	s_nop 1
	v_addc_co_u32_e32 v217, vcc, 0, v207, vcc
	v_add_co_u32_e32 v218, vcc, s17, v206
	s_nop 1
	v_addc_co_u32_e32 v219, vcc, 0, v207, vcc
	v_add_co_u32_e32 v220, vcc, s11, v206
	s_nop 1
	v_addc_co_u32_e32 v221, vcc, 0, v207, vcc
	global_store_dwordx4 v[206:207], v[174:177], off
	global_store_dwordx4 v[206:207], v[170:173], off offset:64
	global_store_dwordx4 v[206:207], v[158:161], off offset:128
	global_store_dwordx4 v[206:207], v[142:145], off offset:192
	global_store_dwordx4 v[208:209], v[166:169], off
	global_store_dwordx4 v[208:209], v[162:165], off offset:64
	global_store_dwordx4 v[208:209], v[146:149], off offset:128
	global_store_dwordx4 v[208:209], v[122:125], off offset:192
	global_store_dwordx4 v[210:211], v[154:157], off
	global_store_dwordx4 v[210:211], v[150:153], off offset:64
	global_store_dwordx4 v[210:211], v[130:133], off offset:128
	global_store_dwordx4 v[210:211], v[106:109], off offset:192
	global_store_dwordx4 v[212:213], v[138:141], off
	global_store_dwordx4 v[212:213], v[134:137], off offset:64
	global_store_dwordx4 v[212:213], v[114:117], off offset:128
	global_store_dwordx4 v[212:213], v[90:93], off offset:192
	global_store_dwordx4 v[214:215], v[126:129], off
	global_store_dwordx4 v[214:215], v[118:121], off offset:64
	global_store_dwordx4 v[214:215], v[98:101], off offset:128
	global_store_dwordx4 v[214:215], v[74:77], off offset:192
	global_store_dwordx4 v[216:217], v[110:113], off
	global_store_dwordx4 v[216:217], v[102:105], off offset:64
	global_store_dwordx4 v[216:217], v[82:85], off offset:128
	global_store_dwordx4 v[216:217], v[62:65], off offset:192
	global_store_dwordx4 v[218:219], v[94:97], off
	global_store_dwordx4 v[218:219], v[86:89], off offset:64
	global_store_dwordx4 v[218:219], v[70:73], off offset:128
	global_store_dwordx4 v[218:219], v[54:57], off offset:192
	global_store_dwordx4 v[220:221], v[78:81], off
	global_store_dwordx4 v[220:221], v[66:69], off offset:64
	global_store_dwordx4 v[220:221], v[58:61], off offset:128
	global_store_dwordx4 v[220:221], v[50:53], off offset:192
	s_waitcnt lgkmcnt(0)
	s_barrier
	s_branch .LBB1_6
.Lfirst:
	v_add_u32_e32 v182, s19, v191
	v_add_u32_e32 v238, s19, v192
	ds_read_b128 v[178:181], v182 offset:32768
	ds_read_b128 v[194:197], v182 offset:34816
	ds_read_b128 v[198:201], v182 offset:36864
	ds_read_b128 v[202:205], v182 offset:38912
	ds_read_b128 v[206:209], v238
	ds_read_b128 v[210:213], v238 offset:2048
	ds_read_b128 v[214:217], v238 offset:4096
	ds_read_b128 v[218:221], v238 offset:6144
	ds_read_b128 v[222:225], v238 offset:8192
	ds_read_b128 v[226:229], v238 offset:10240
	ds_read_b128 v[230:233], v238 offset:12288
	ds_read_b128 v[234:237], v238 offset:14336
	s_min_u32 s21, s20, 29
	s_xor_b32 s19, s19, 0x10000
	v_add_u32_e32 v239, s19, v189
	s_waitcnt vmcnt(11)
	v_cvt_pk_bf16_f32 v13, v12, v13
	v_cvt_pk_bf16_f32 v12, v10, v11
	s_waitcnt vmcnt(10)
	v_cvt_pk_bf16_f32 v11, v20, v21
	v_cvt_pk_bf16_f32 v10, v18, v19
	ds_write2st64_b64 v239, v[12:13], v[10:11] offset1:8
	s_waitcnt vmcnt(9)
	v_cvt_pk_bf16_f32 v11, v24, v25
	v_cvt_pk_bf16_f32 v10, v22, v23
	s_waitcnt vmcnt(8)
	v_cvt_pk_bf16_f32 v13, v32, v33
	v_cvt_pk_bf16_f32 v12, v30, v31
	ds_write2st64_b64 v239, v[10:11], v[12:13] offset0:16 offset1:24
	s_waitcnt vmcnt(7)
	v_cvt_pk_bf16_f32 v11, v36, v37
	v_cvt_pk_bf16_f32 v10, v34, v35
	s_waitcnt vmcnt(6)
	v_cvt_pk_bf16_f32 v13, v40, v41
	v_cvt_pk_bf16_f32 v12, v38, v39
	ds_write2st64_b64 v239, v[10:11], v[12:13] offset0:32 offset1:40
	s_waitcnt vmcnt(5)
	v_cvt_pk_bf16_f32 v11, v44, v45
	v_cvt_pk_bf16_f32 v10, v42, v43
	s_waitcnt vmcnt(4)
	v_cvt_pk_bf16_f32 v13, v48, v49
	v_cvt_pk_bf16_f32 v12, v46, v47
	ds_write2st64_b64 v239, v[10:11], v[12:13] offset0:48 offset1:56
	s_waitcnt lgkmcnt(0)
	s_add_i32 s21, s21, 2
	s_barrier
	s_waitcnt lgkmcnt(11)
	v_mfma_f32_16x16x32_bf16 v[174:177], v[178:181], v[206:209], v[240:243]
	s_lshl_b32 s22, s21, 1
	s_and_b32 s22, s22, 0x60
	s_add_i32 s22, s22, s12
	s_lshl_b32 s22, s22, 6
	v_mfma_f32_16x16x32_bf16 v[170:173], v[194:197], v[206:209], v[244:247]
	s_and_b32 s22, s22, 0x3f00
	s_or_b32 s22, s22, s13
	s_lshl_b32 s23, s21, 23
	s_lshl_b32 s22, s22, 9
	v_mfma_f32_16x16x32_bf16 v[158:161], v[198:201], v[206:209], v[248:251]
	s_and_b32 s23, s23, 0x7000000
	s_or_b32 s22, s22, s23
	s_lshl_b32 s23, s21, 8
	s_and_b32 s23, s23, 0x100
	s_or_b32 s22, s22, s23
	s_or_b32 s23, s22, 0x4000
	buffer_load_dwordx4 v[10:13], v1, s[4:7], s22 offen sc0 nt
	v_mfma_f32_16x16x32_bf16 v[142:145], v[202:205], v[206:209], v[252:255]
	ds_read_b128 v[206:209], v238 offset:1024
	s_waitcnt lgkmcnt(10)
	v_mfma_f32_16x16x32_bf16 v[166:169], v[178:181], v[210:213], v[240:243]
	v_mfma_f32_16x16x32_bf16 v[162:165], v[194:197], v[210:213], v[244:247]
	v_mfma_f32_16x16x32_bf16 v[146:149], v[198:201], v[210:213], v[248:251]
	buffer_load_dwordx4 v[18:21], v1, s[4:7], s23 offen sc0 nt
	s_or_b32 s23, s22, 0x8000
	v_mfma_f32_16x16x32_bf16 v[122:125], v[202:205], v[210:213], v[252:255]
	ds_read_b128 v[210:213], v238 offset:3072
	s_waitcnt lgkmcnt(9)
	v_mfma_f32_16x16x32_bf16 v[154:157], v[178:181], v[214:217], v[240:243]
	v_mfma_f32_16x16x32_bf16 v[150:153], v[194:197], v[214:217], v[244:247]
	v_mfma_f32_16x16x32_bf16 v[130:133], v[198:201], v[214:217], v[248:251]
	buffer_load_dwordx4 v[22:25], v1, s[4:7], s23 offen sc0 nt
	s_or_b32 s23, s22, 0xc000
	v_mfma_f32_16x16x32_bf16 v[106:109], v[202:205], v[214:217], v[252:255]
	ds_read_b128 v[214:217], v238 offset:5120
	s_waitcnt lgkmcnt(8)
	v_mfma_f32_16x16x32_bf16 v[138:141], v[178:181], v[218:221], v[240:243]
	v_mfma_f32_16x16x32_bf16 v[134:137], v[194:197], v[218:221], v[244:247]
	v_mfma_f32_16x16x32_bf16 v[114:117], v[198:201], v[218:221], v[248:251]
	buffer_load_dwordx4 v[30:33], v1, s[4:7], s23 offen sc0 nt
	s_or_b32 s23, s22, 0x10000
	v_mfma_f32_16x16x32_bf16 v[90:93], v[202:205], v[218:221], v[252:255]
	ds_read_b128 v[218:221], v238 offset:7168
	s_waitcnt lgkmcnt(7)
	v_mfma_f32_16x16x32_bf16 v[126:129], v[178:181], v[222:225], v[240:243]
	v_mfma_f32_16x16x32_bf16 v[118:121], v[194:197], v[222:225], v[244:247]
	v_mfma_f32_16x16x32_bf16 v[98:101], v[198:201], v[222:225], v[248:251]
	buffer_load_dwordx4 v[34:37], v1, s[4:7], s23 offen sc0 nt
	s_or_b32 s23, s22, 0x14000
	v_mfma_f32_16x16x32_bf16 v[74:77], v[202:205], v[222:225], v[252:255]
	ds_read_b128 v[222:225], v238 offset:9216
	s_waitcnt lgkmcnt(6)
	v_mfma_f32_16x16x32_bf16 v[110:113], v[178:181], v[226:229], v[240:243]
	v_mfma_f32_16x16x32_bf16 v[102:105], v[194:197], v[226:229], v[244:247]
	v_mfma_f32_16x16x32_bf16 v[82:85], v[198:201], v[226:229], v[248:251]
	buffer_load_dwordx4 v[38:41], v1, s[4:7], s23 offen sc0 nt
	s_or_b32 s23, s22, 0x18000
	s_or_b32 s22, s22, 0x1c000
	v_mfma_f32_16x16x32_bf16 v[62:65], v[202:205], v[226:229], v[252:255]
	ds_read_b128 v[226:229], v238 offset:11264
	s_waitcnt lgkmcnt(5)
	v_mfma_f32_16x16x32_bf16 v[94:97], v[178:181], v[230:233], v[240:243]
	v_mfma_f32_16x16x32_bf16 v[86:89], v[194:197], v[230:233], v[244:247]
	v_mfma_f32_16x16x32_bf16 v[70:73], v[198:201], v[230:233], v[248:251]
	buffer_load_dwordx4 v[42:45], v1, s[4:7], s23 offen sc0 nt
	v_mfma_f32_16x16x32_bf16 v[54:57], v[202:205], v[230:233], v[252:255]
	s_waitcnt lgkmcnt(4)
	v_mfma_f32_16x16x32_bf16 v[78:81], v[178:181], v[234:237], v[240:243]
	v_mfma_f32_16x16x32_bf16 v[66:69], v[194:197], v[234:237], v[244:247]
	v_mfma_f32_16x16x32_bf16 v[58:61], v[198:201], v[234:237], v[248:251]
	buffer_load_dwordx4 v[46:49], v1, s[4:7], s22 offen sc0 nt
	v_mfma_f32_16x16x32_bf16 v[50:53], v[202:205], v[234:237], v[252:255]
	s_waitcnt lgkmcnt(0)
	s_barrier
	ds_read_b128 v[178:181], v182 offset:33792
	ds_read_b128 v[194:197], v182 offset:35840
	ds_read_b128 v[198:201], v182 offset:37888
	ds_read_b128 v[202:205], v182 offset:39936
	ds_read_b128 v[230:233], v238 offset:13312
	ds_read_b128 v[234:237], v238 offset:15360
	v_add_u32_e32 v182, s19, v190
	s_waitcnt vmcnt(11)
	ds_write_b128 v182, v[2:5] offset:32768
	s_waitcnt vmcnt(10)
	ds_write_b128 v182, v[6:9] offset:40960
	s_waitcnt vmcnt(9)
	ds_write_b128 v182, v[14:17] offset:49152
	s_waitcnt vmcnt(8)
	ds_write_b128 v182, v[26:29] offset:57344
	s_waitcnt lgkmcnt(0)
	s_barrier
	s_waitcnt lgkmcnt(11)
	v_mfma_f32_16x16x32_bf16 v[174:177], v[178:181], v[206:209], v[174:177]
	s_lshl_b32 s21, s21, 15
	s_and_b32 s21, s21, 0x78000
	s_or_b32 s21, s21, s14
	s_or_b32 s22, s21, 0x2000
	v_mfma_f32_16x16x32_bf16 v[170:173], v[194:197], v[206:209], v[170:173]
	v_mfma_f32_16x16x32_bf16 v[158:161], v[198:201], v[206:209], v[158:161]
	v_mfma_f32_16x16x32_bf16 v[142:145], v[202:205], v[206:209], v[142:145]
	s_waitcnt lgkmcnt(10)
	v_mfma_f32_16x16x32_bf16 v[166:169], v[178:181], v[210:213], v[166:169]
	v_mfma_f32_16x16x32_bf16 v[162:165], v[194:197], v[210:213], v[162:165]
	buffer_load_dwordx4 v[2:5], v188, s[0:3], s21 offen sc1
	v_mfma_f32_16x16x32_bf16 v[146:149], v[198:201], v[210:213], v[146:149]
	v_mfma_f32_16x16x32_bf16 v[122:125], v[202:205], v[210:213], v[122:125]
	s_waitcnt lgkmcnt(9)
	v_mfma_f32_16x16x32_bf16 v[154:157], v[178:181], v[214:217], v[154:157]
	v_mfma_f32_16x16x32_bf16 v[150:153], v[194:197], v[214:217], v[150:153]
	v_mfma_f32_16x16x32_bf16 v[130:133], v[198:201], v[214:217], v[130:133]
	v_mfma_f32_16x16x32_bf16 v[106:109], v[202:205], v[214:217], v[106:109]
	s_waitcnt lgkmcnt(8)
	v_mfma_f32_16x16x32_bf16 v[138:141], v[178:181], v[218:221], v[138:141]
	v_mfma_f32_16x16x32_bf16 v[134:137], v[194:197], v[218:221], v[134:137]
	buffer_load_dwordx4 v[6:9], v188, s[0:3], s22 offen sc1
	s_or_b32 s22, s21, 0x4000
	s_or_b32 s21, s21, 0x6000
	v_mfma_f32_16x16x32_bf16 v[114:117], v[198:201], v[218:221], v[114:117]
	v_mfma_f32_16x16x32_bf16 v[90:93], v[202:205], v[218:221], v[90:93]
	s_waitcnt lgkmcnt(7)
	v_mfma_f32_16x16x32_bf16 v[126:129], v[178:181], v[222:225], v[126:129]
	v_mfma_f32_16x16x32_bf16 v[118:121], v[194:197], v[222:225], v[118:121]
	v_mfma_f32_16x16x32_bf16 v[98:101], v[198:201], v[222:225], v[98:101]
	v_mfma_f32_16x16x32_bf16 v[74:77], v[202:205], v[222:225], v[74:77]
	s_waitcnt lgkmcnt(6)
	v_mfma_f32_16x16x32_bf16 v[110:113], v[178:181], v[226:229], v[110:113]
	v_mfma_f32_16x16x32_bf16 v[102:105], v[194:197], v[226:229], v[102:105]
	buffer_load_dwordx4 v[14:17], v188, s[0:3], s22 offen sc1
	v_mfma_f32_16x16x32_bf16 v[82:85], v[198:201], v[226:229], v[82:85]
	v_mfma_f32_16x16x32_bf16 v[62:65], v[202:205], v[226:229], v[62:65]
	s_waitcnt lgkmcnt(5)
	v_mfma_f32_16x16x32_bf16 v[94:97], v[178:181], v[230:233], v[94:97]
	v_mfma_f32_16x16x32_bf16 v[86:89], v[194:197], v[230:233], v[86:89]
	v_mfma_f32_16x16x32_bf16 v[70:73], v[198:201], v[230:233], v[70:73]
	v_mfma_f32_16x16x32_bf16 v[54:57], v[202:205], v[230:233], v[54:57]
	s_waitcnt lgkmcnt(4)
	v_mfma_f32_16x16x32_bf16 v[78:81], v[178:181], v[234:237], v[78:81]
	v_mfma_f32_16x16x32_bf16 v[66:69], v[194:197], v[234:237], v[66:69]
	buffer_load_dwordx4 v[26:29], v188, s[0:3], s21 offen sc1
	v_mfma_f32_16x16x32_bf16 v[58:61], v[198:201], v[234:237], v[58:61]
	v_mfma_f32_16x16x32_bf16 v[50:53], v[202:205], v[234:237], v[50:53]
	s_branch .LBB1_3
